# v21 = v20 + workgroups 128..255 run phase 5 in the opposite order (attention first, then RWKV scan)
# baseline (speedup 1.0000x reference)
; #define RUN(grp, ...) do { for (int rep_ = 0; rep_ < ((PROBE == (grp)) ? 2 : 1); ++rep_) { __VA_ARGS__ } } while (0)
; __global__ void __launch_bounds__(NTHR, 2) k_all(Params p) {
;     ...
;     RUN(3, ph_rwscan(p, lds, wg, nwg, ct_split); ph_naattn(p, lds, wg, nwg);); xcd_barrier(bar);
.LBB0_606:
	s_or_b64 exec, exec, s[0:1]
	v_writelane_b32 v249, s6, 0
	v_writelane_b32 v249, s12, 1
	v_writelane_b32 v249, s14, 2
	v_writelane_b32 v249, s15, 3
	v_writelane_b32 v249, s18, 4
	v_writelane_b32 v249, s19, 5
	v_writelane_b32 v249, s20, 6
	v_writelane_b32 v249, s21, 7
	v_writelane_b32 v249, s22, 8
	v_writelane_b32 v249, s23, 9
	v_writelane_b32 v249, s24, 10
	v_writelane_b32 v249, s25, 11
	v_writelane_b32 v249, s34, 12
	v_writelane_b32 v249, s35, 13
	v_writelane_b32 v249, s39, 14
	v_writelane_b32 v249, s46, 15
	v_writelane_b32 v249, s47, 16
	v_writelane_b32 v249, s48, 17
	v_writelane_b32 v249, s49, 18
	v_writelane_b32 v249, s74, 19
	v_writelane_b32 v249, s75, 20
	v_writelane_b32 v249, s76, 21
	v_writelane_b32 v249, s77, 22
	v_writelane_b32 v249, s88, 23
	v_writelane_b32 v249, s90, 24
	v_writelane_b32 v249, s91, 25
	v_writelane_b32 v249, s92, 26
	v_writelane_b32 v249, s93, 27
	v_writelane_b32 v249, s96, 28
	v_writelane_b32 v249, s97, 29
	v_mov_b32_e32 v250, v5
	v_mov_b32_e32 v251, v245
	v_mov_b32_e32 v252, v248
	s_bfe_u32 s98, s90, 0x10007
	s_mov_b32 s99, 0
	v_writelane_b32 v249, s98, 60
	v_writelane_b32 v249, s99, 61
	v_writelane_b32 v249, s98, 62
